# v36 + MoE1: workgroup groups with bid bit 5 set start the phase ~6 us later (s_sleep), so half of each XCD's sibling groups reach their unit epilogue/prologue while the other half streams weights
# baseline (speedup 1.0000x reference)
.LBB0_1417:
	s_cmp_lt_i32 s92, 12
	s_cselect_b64 s[8:9], -1, 0
	s_and_b64 s[0:1], s[8:9], s[0:1]
	s_andn2_b64 vcc, exec, s[0:1]
	s_cbranch_vccnz .LBB0_1482
	s_bitcmp1_b32 s96, 5
	s_cbranch_scc0 .Lstag_m1
	s_sleep 100
	s_sleep 100
.Lstag_m1:
	s_and_b32 s2, s96, 7
	s_ashr_i32 s3, s72, 3
	s_mul_i32 s2, s2, s3
	s_ashr_i32 s5, s96, 3
	s_and_b32 s4, s72, 7
	s_add_i32 s6, s5, s2
	s_and_b32 s2, s96, 4
	s_bfe_i32 s3, s96, 0x10002
	s_bitcmp1_b32 s96, 2
	s_cselect_b64 s[12:13], -1, 0
	s_lshl_b32 s7, s96, 5
	s_and_b32 s7, s7, 0xe0
	s_add_i32 s7, s5, s7
	s_cmp_eq_u32 s2, 0
	s_cselect_b64 s[14:15], -1, 0
	s_and_b32 s42, s3, 0x480
	s_add_u32 s16, s70, 0x140b8000
	s_addc_u32 s17, s71, 0
	s_add_u32 s18, s70, 0x12038000
	v_lshrrev_b32_e32 v192, 4, v170
	v_lshrrev_b32_e32 v195, 1, v0
	s_waitcnt vmcnt(23)
	v_bfe_u32 v3, v0, 1, 3
	s_addc_u32 s19, s71, 0
	v_bitop3_b32 v4, v192, v195, 7 bitop3:0x78
	v_bitop3_b32 v3, v192, v3, 4 bitop3:0x36
	s_add_u32 s43, s70, 0x14158000
	v_lshlrev_b32_e32 v196, 4, v4
	v_lshlrev_b32_e32 v197, 4, v3
	v_bfe_u32 v3, v0, 2, 2
	v_lshrrev_b32_e32 v4, 2, v170
	s_addc_u32 s44, s71, 0
	s_waitcnt vmcnt(7)
	v_lshrrev_b32_e32 v6, 4, v0
	v_and_or_b32 v4, v4, 4, v3
	s_add_u32 s45, s70, 0x7038000
	v_xor_b32_e32 v6, v6, v0
	v_lshrrev_b32_e32 v193, 5, v170
	v_lshlrev_b32_e32 v198, 5, v4
	v_lshlrev_b32_e32 v4, 3, v0
	s_addc_u32 s46, s71, 0
	v_lshlrev_b32_e32 v6, 3, v6
	v_and_b32_e32 v2, 31, v0
	v_and_b32_e32 v8, 24, v4
	v_mul_u32_u24_e32 v4, 0x2c00, v193
	s_add_u32 s47, s70, 0x4000
	v_and_b32_e32 v201, 56, v6
	v_and_b32_e32 v6, 2, v0
	v_lshl_or_b32 v199, v2, 4, v4
	s_addc_u32 s48, s71, 0
	s_ashr_i32 s2, s7, 5
	v_lshlrev_b32_e32 v4, 6, v0
	v_mov_b32_e32 v7, s63
	v_mov_b32_e32 v9, s61
	v_cmp_eq_u32_e32 vcc, 0, v6
	s_mul_hi_i32 s3, s2, 0x1600000
	s_mul_i32 s2, s2, 0x1600000
	v_and_b32_e32 v4, 64, v4
	v_cndmask_b32_e32 v177, v7, v9, vcc
	v_mov_b32_e32 v6, s62
	v_mov_b32_e32 v7, s60
	v_mov_b32_e32 v173, 0
	s_add_u32 s2, s64, s2
	v_lshlrev_b32_e32 v172, 1, v4
	v_cndmask_b32_e32 v176, v6, v7, vcc
	v_lshlrev_b32_e32 v6, 12, v0
	s_addc_u32 s3, s65, s3
	s_lshl_b32 s5, s5, 8
	v_lshl_add_u64 v[174:175], s[18:19], 0, v[172:173]
	v_and_b32_e32 v172, 0x1fe000, v6
	v_and_b32_e32 v1, 15, v0
	s_mov_b32 s11, 0
	s_and_b32 s10, s5, 0x1c00
	v_lshl_add_u64 v[6:7], s[2:3], 0, v[172:173]
	v_lshlrev_b32_e32 v9, 9, v0
	v_lshrrev_b32_e32 v171, 3, v0
	s_movk_i32 s0, 0x70
	v_lshlrev_b32_e32 v194, 3, v2
	v_lshlrev_b32_e32 v5, 12, v192
	v_lshlrev_b32_e32 v3, 9, v3
	v_lshlrev_b32_e32 v2, 3, v1
	s_cmp_eq_u32 s4, 0
	v_lshl_add_u64 v[6:7], v[6:7], 0, s[10:11]
	v_and_b32_e32 v172, 0x200, v9
	v_bitop3_b32 v190, v158, s0, v0 bitop3:0x48
	v_or_b32_e32 v191, 0x80, v171
	v_cmp_eq_u32_e64 s[0:1], 0, v0
	v_or_b32_e32 v202, 0xc0, v171
	v_lshl_add_u64 v[178:179], v[6:7], 0, v[172:173]
	s_cselect_b32 s49, s6, s96
	s_cselect_b32 s50, s7, s96
	v_or3_b32 v203, v5, v3, v8
	s_mov_b64 s[2:3], 0
	v_lshlrev_b32_e32 v180, 2, v4
	s_mov_b64 s[20:21], 0x80
	s_movk_i32 s51, 0xff
	s_add_i32 s52, 0, 0x18000
	s_mov_b32 s53, 0x10000
	s_add_i32 s56, 0, 0x20000
	s_movk_i32 s57, 0x110
	s_mov_b32 s10, 0xbfb8aa3b
	v_lshlrev_b32_e32 v182, 1, v2
	s_movk_i32 s58, 0x1600
	s_mov_b64 s[22:23], 0x10000
	v_mov_b32_e32 v208, 0
	v_mov_b32_e32 v209, 0
	v_mov_b32_e32 v210, 0
	v_mov_b32_e32 v211, 0
	s_branch .LBB0_1422
